# MLA row sums (first half-step, both copies): last 16 addends summed with 7 v_pk_add_f32 + 2 adds instead of 16 serial adds (f32 kept; association order of the sum changes)
# baseline (speedup 1.0000x reference)
; __device__ __forceinline__ void finishSM(f32x16& p0, f32x16& p1, float alpha, float& l_reg, bf16x8& pa0, bf16x8& pa1, bf16x8& pa2, bf16x8& pa3) {
; #pragma unroll
;     for (int r = 0; r < 16; ++r) p1[r] = __builtin_amdgcn_exp2f(p1[r]);
;     float ps = 0;
; #pragma unroll
;     for (int r = 0; r < 16; ++r) ps += p0[r];
; #pragma unroll
;     for (int r = 0; r < 16; ++r) ps += p1[r];
;     { auto rr = __builtin_amdgcn_permlane32_swap(__float_as_uint(ps), __float_as_uint(ps), false, false);
;       ps = __uint_as_float(rr[0]) + __uint_as_float(rr[1]); }
;     l_reg = l_reg * alpha + ps;
;     ...
;     PK4(p0, 0, pa0); PK4(p0, 8, pa1); PK4(p1, 0, pa2); PK4(p1, 8, pa3);
; template <int KB, bool SK, bool ROPE, bool QHALF>
; __device__ __forceinline__ void qkt(f32x16& p0, f32x16& p1, const char* lds, int r32, int hi, const bf16x8* qr, const char* qrl, bool act) {
;     ...
;     const char* kb[4];
; #pragma unroll
;     for (int dd = 0; dd < 4; ++dd) kb[dd] = lds + OFF_K + KB * SHM_K + KSWZ(r32, (dd * 16 + hi * 8) * 2);
; #pragma unroll
;     for (int d0 = 0; d0 < 8; ++d0) { const char* a = kb[d0 & 3] + (d0 >> 2) * 128;
;         bf16x8 b0 = *reinterpret_cast<const bf16x8*>(a);
;         bf16x8 b1 = *reinterpret_cast<const bf16x8*>(a + 32 * 256);
;         bf16x8 qf;
;         if constexpr (QHALF) { if (d0 >= 4) qf = *reinterpret_cast<const bf16x8*>(qrl + (d0 - 4) * 1024); else qf = qr[d0]; } else qf = qr[d0];
;         p0 = __builtin_amdgcn_mfma_f32_32x32x16_bf16(b0, qf, p0, 0, 0, 0);
;         p1 = __builtin_amdgcn_mfma_f32_32x32x16_bf16(b1, qf, p1, 0, 0, 0); }
;     if constexpr (ROPE) {
; #pragma unroll
;         for (int d0 = 0; d0 < 4; ++d0) { const char* a = lds + OFF_KR + KB * SHM_KR + KRSWZ(r32, 2 * d0 + hi);
;             bf16x8 b0 = *reinterpret_cast<const bf16x8*>(a);
;             bf16x8 b1 = *reinterpret_cast<const bf16x8*>(a + 32 * 128);
;             const bf16x8 qf = *reinterpret_cast<const bf16x8*>(qrl + d0 * 1024);
;             p0 = __builtin_amdgcn_mfma_f32_32x32x16_bf16(b0, qf, p0, 0, 0, 0);
;             p1 = __builtin_amdgcn_mfma_f32_32x32x16_bf16(b1, qf, p1, 0, 0, 0); }
.Lmy_nobar_0:
.LBB0_525:
	ds_read_b128 v[4:7], v213 offset:49152
	ds_read_b128 v[8:11], v213 offset:57344
	s_add_i32 s10, 0, 0x12800
	v_exp_f32_e32 v122, v132
	v_exp_f32_e32 v123, v133
	s_waitcnt lgkmcnt(1)
	v_mfma_f32_32x32x16_bf16 v[102:117], v[4:7], v[174:177], 0
	v_exp_f32_e32 v124, v130
	v_exp_f32_e32 v125, v131
	v_exp_f32_e32 v126, v126
	v_exp_f32_e32 v127, v127
	v_exp_f32_e32 v128, v128
	v_exp_f32_e32 v129, v129
	s_add_i32 s6, s48, 0xffffff60
	s_waitcnt lgkmcnt(0)
	v_mfma_f32_32x32x16_bf16 v[86:101], v[8:11], v[174:177], 0
	ds_read_b128 v[4:7], v214 offset:49152
	ds_read_b128 v[8:11], v214 offset:57344
	s_add_i32 s7, s48, 0xffffff9f
	s_waitcnt lgkmcnt(1)
	v_mfma_f32_32x32x16_bf16 v[102:117], v[4:7], v[170:173], v[102:117]
	s_waitcnt lgkmcnt(0)
	v_mfma_f32_32x32x16_bf16 v[86:101], v[8:11], v[170:173], v[86:101]
	ds_read_b128 v[4:7], v215 offset:49152
	ds_read_b128 v[8:11], v215 offset:57344
	s_waitcnt lgkmcnt(1)
	v_mfma_f32_32x32x16_bf16 v[102:117], v[4:7], v[166:169], v[102:117]
	s_waitcnt lgkmcnt(0)
	v_mfma_f32_32x32x16_bf16 v[86:101], v[8:11], v[166:169], v[86:101]
	ds_read_b128 v[4:7], v216 offset:49152
	ds_read_b128 v[8:11], v216 offset:57344
	s_waitcnt lgkmcnt(1)
	v_mfma_f32_32x32x16_bf16 v[102:117], v[4:7], v[162:165], v[102:117]
	s_waitcnt lgkmcnt(0)
	v_mfma_f32_32x32x16_bf16 v[86:101], v[8:11], v[162:165], v[86:101]
	ds_read_b128 v[4:7], v213 offset:49280
	ds_read_b128 v[8:11], v213 offset:57472
	s_waitcnt lgkmcnt(1)
	v_mfma_f32_32x32x16_bf16 v[102:117], v[4:7], v[158:161], v[102:117]
	s_waitcnt lgkmcnt(0)
	v_mfma_f32_32x32x16_bf16 v[86:101], v[8:11], v[158:161], v[86:101]
	ds_read_b128 v[4:7], v214 offset:49280
	ds_read_b128 v[8:11], v214 offset:57472
	s_waitcnt lgkmcnt(1)
	v_mfma_f32_32x32x16_bf16 v[102:117], v[4:7], v[154:157], v[102:117]
	s_waitcnt lgkmcnt(0)
	v_mfma_f32_32x32x16_bf16 v[86:101], v[8:11], v[154:157], v[86:101]
	ds_read_b128 v[4:7], v215 offset:49280
	ds_read_b128 v[8:11], v215 offset:57472
	s_waitcnt lgkmcnt(1)
	v_mfma_f32_32x32x16_bf16 v[102:117], v[4:7], v[150:153], v[102:117]
	s_waitcnt lgkmcnt(0)
	v_mfma_f32_32x32x16_bf16 v[86:101], v[8:11], v[150:153], v[86:101]
	ds_read_b128 v[4:7], v216 offset:49280
	ds_read_b128 v[8:11], v216 offset:57472
	s_waitcnt lgkmcnt(1)
	v_mfma_f32_32x32x16_bf16 v[102:117], v[4:7], v[146:149], v[102:117]
	s_waitcnt lgkmcnt(0)
	v_mfma_f32_32x32x16_bf16 v[86:101], v[8:11], v[146:149], v[86:101]
	v_add_u32_e32 v8, s10, v217
	ds_read_b128 v[4:7], v8
	ds_read_b128 v[8:11], v8 offset:4096
	ds_read_b128 v[12:15], v202
	s_waitcnt lgkmcnt(0)
	v_mfma_f32_32x32x16_bf16 v[102:117], v[4:7], v[12:15], v[102:117]
	v_mfma_f32_32x32x16_bf16 v[86:101], v[8:11], v[12:15], v[86:101]
	v_add_u32_e32 v8, s10, v218
	ds_read_b128 v[4:7], v8
	ds_read_b128 v[8:11], v8 offset:4096
	ds_read_b128 v[12:15], v202 offset:1024
	s_waitcnt lgkmcnt(0)
	v_mfma_f32_32x32x16_bf16 v[102:117], v[4:7], v[12:15], v[102:117]
	v_mfma_f32_32x32x16_bf16 v[86:101], v[8:11], v[12:15], v[86:101]
	v_add_u32_e32 v8, s10, v219
	ds_read_b128 v[4:7], v8
	ds_read_b128 v[8:11], v8 offset:4096
	ds_read_b128 v[12:15], v202 offset:2048
	s_waitcnt lgkmcnt(0)
	v_mfma_f32_32x32x16_bf16 v[102:117], v[4:7], v[12:15], v[102:117]
	v_mfma_f32_32x32x16_bf16 v[86:101], v[8:11], v[12:15], v[86:101]
	v_add_u32_e32 v8, s10, v220
	ds_read_b128 v[4:7], v8
	ds_read_b128 v[8:11], v8 offset:4096
	ds_read_b128 v[12:15], v202 offset:3072
	s_waitcnt lgkmcnt(0)
	v_mfma_f32_32x32x16_bf16 v[102:117], v[4:7], v[12:15], v[102:117]
	v_exp_f32_e32 v4, v140
	v_exp_f32_e32 v5, v141
	v_exp_f32_e32 v6, v138
	v_exp_f32_e32 v7, v139
	v_mfma_f32_32x32x16_bf16 v[86:101], v[8:11], v[12:15], v[86:101]
	ds_read_b64_tr_b16 v[232:233], v210 offset:0
	ds_read_b64_tr_b16 v[234:235], v210 offset:0x800
	ds_read_b64_tr_b16 v[236:237], v210 offset:0x1000
	ds_read_b64_tr_b16 v[238:239], v210 offset:0x1800
	ds_read_b64_tr_b16 v[240:241], v210 offset:0x2000
	ds_read_b64_tr_b16 v[242:243], v210 offset:0x2800
	ds_read_b64_tr_b16 v[244:245], v210 offset:0x3000
	ds_read_b64_tr_b16 v[246:247], v210 offset:0x3800
	v_add_f32_e32 v12, 0, v188
	v_add_f32_e32 v12, v228, v12
	v_add_f32_e32 v12, v186, v12
	v_add_f32_e32 v12, v189, v12
	v_add_f32_e32 v12, v185, v12
	v_add_f32_e32 v12, v187, v12
	v_add_f32_e32 v12, v183, v12
	v_add_f32_e32 v12, v184, v12
	v_add_f32_e32 v12, v179, v12
	v_add_f32_e32 v12, v182, v12
	v_add_f32_e32 v12, v144, v12
	v_add_f32_e32 v12, v180, v12
	v_add_f32_e32 v12, v142, v12
	v_add_f32_e32 v12, v181, v12
	v_add_f32_e32 v12, v143, v12
	v_add_f32_e32 v12, v145, v12
	v_exp_f32_e32 v8, v136
	v_exp_f32_e32 v9, v137
	v_exp_f32_e32 v10, v134
	v_exp_f32_e32 v11, v135
	v_pk_add_f32 v[14:15], v[4:5], v[6:7]
	v_pk_add_f32 v[14:15], v[14:15], v[8:9]
	v_pk_add_f32 v[14:15], v[14:15], v[10:11]
	v_pk_add_f32 v[14:15], v[14:15], v[122:123]
	v_pk_add_f32 v[14:15], v[14:15], v[124:125]
	v_pk_add_f32 v[14:15], v[14:15], v[126:127]
	v_pk_add_f32 v[14:15], v[14:15], v[128:129]
	v_add_f32_e32 v12, v14, v12
	v_add_f32_e32 v195, v15, v12
	v_mov_b32_e32 v226, v195
	s_nop 1
	v_permlane32_swap_b32_e32 v195, v226
	v_cvt_pk_bf16_f32 v12, v188, v228
	v_cvt_pk_bf16_f32 v13, v186, v189
	v_cvt_pk_bf16_f32 v14, v185, v187
	v_cvt_pk_bf16_f32 v15, v183, v184
	v_cvt_pk_bf16_f32 v82, v179, v182
	v_cvt_pk_bf16_f32 v83, v144, v180
	v_cvt_pk_bf16_f32 v84, v142, v181
	v_cvt_pk_bf16_f32 v85, v143, v145
	v_cvt_pk_bf16_f32 v118, v4, v5
	v_cvt_pk_bf16_f32 v119, v6, v7
	v_cvt_pk_bf16_f32 v120, v8, v9
	v_cvt_pk_bf16_f32 v121, v10, v11
	v_cvt_pk_bf16_f32 v122, v122, v123
	v_cvt_pk_bf16_f32 v123, v124, v125
	v_cvt_pk_bf16_f32 v124, v126, v127
	v_cvt_pk_bf16_f32 v125, v128, v129
	s_nop 0
	v_permlane32_swap_b32_e32 v12, v14
	v_permlane32_swap_b32_e32 v13, v15
	v_permlane32_swap_b32_e32 v82, v84
	v_permlane32_swap_b32_e32 v83, v85
	v_permlane32_swap_b32_e32 v118, v120
	v_permlane32_swap_b32_e32 v119, v121
	v_permlane32_swap_b32_e32 v122, v124
	v_permlane32_swap_b32_e32 v123, v125
	s_add_i32 s10, s48, 0xffffffa0
	s_sub_i32 s72, s48, 64
	s_mov_b32 s73, s11
	s_lshl_b64 s[50:51], s[10:11], 12
	s_lshl_b64 s[72:73], s[72:73], 12
	v_lshl_add_u64 v[4:5], v[196:197], 0, s[50:51]
	v_lshl_add_u64 v[8:9], v[196:197], 0, s[72:73]
	v_lshl_add_u64 v[126:127], v[198:199], 0, s[50:51]
	s_add_i32 m0, s37, 0x8000
	global_load_dwordx4 v[4:7], v[4:5], off
	s_nop 0
	global_load_dwordx4 v[8:11], v[8:9], off
	s_lshl_b64 s[50:51], s[10:11], 7
	global_load_lds_dwordx4 v[126:127], off
	v_lshl_add_u64 v[126:127], v[198:199], 0, s[72:73]
	s_add_i32 m0, s37, 0xa000
	s_nop 0
	global_load_lds_dwordx4 v[126:127], off
	v_lshl_add_u64 v[126:127], v[16:17], 0, s[50:51]
	s_add_i32 m0, s37, 0x10800
	s_nop 0
	global_load_lds_dwordx4 v[126:127], off
	s_waitcnt lgkmcnt(0)
; __device__ __forceinline__ void mask_tile(f32x16& p0, f32x16& p1, int dq, unsigned W) {
;     const float NEG = -__builtin_inff();
; #pragma unroll
;     for (int r = 0; r < 16; ++r) {
;         const int c = (r & 3) + 8 * (r >> 2);
;         if ((unsigned)(dq - c) >= W) p0[r] = NEG;
;         if ((unsigned)(dq - c - 32) >= W) p1[r] = NEG;
;     }
; }
; template <int VB, bool SK>
; __device__ __forceinline__ void pv_tile(f32x16* o, int vb0, bf16x8 pa0, bf16x8 pa1, bf16x8 pa2, bf16x8 pa3, bool act) {
;     if (SK && !act) return;
;     ...
;     if (ATT_PRIO) __builtin_amdgcn_s_setprio(1);
;     PV_D0(0); PV_D0(1); PV_D0(2); PV_D0(3);
	s_nop 0
	v_mfma_f32_32x32x16_bf16 v[66:81], v[12:15], v[232:235], v[66:81]
	ds_read_b64_tr_b16 v[126:127], v210 offset:0x200
	ds_read_b64_tr_b16 v[128:129], v210 offset:0xa00
	v_mfma_f32_32x32x16_bf16 v[66:81], v[82:85], v[236:239], v[66:81]
	ds_read_b64_tr_b16 v[130:131], v210 offset:0x1200
	ds_read_b64_tr_b16 v[132:133], v210 offset:0x1a00
	v_mfma_f32_32x32x16_bf16 v[66:81], v[118:121], v[240:243], v[66:81]
	ds_read_b64_tr_b16 v[134:135], v210 offset:0x2200
	ds_read_b64_tr_b16 v[136:137], v210 offset:0x2a00
	ds_read_b64_tr_b16 v[142:143], v210 offset:0x3200
	ds_read_b64_tr_b16 v[144:145], v210 offset:0x3a00
	s_waitcnt lgkmcnt(0)
	v_mfma_f32_32x32x16_bf16 v[66:81], v[122:125], v[244:247], v[66:81]
	v_mfma_f32_32x32x16_bf16 v[50:65], v[12:15], v[126:129], v[50:65]
	ds_read_b64_tr_b16 v[126:127], v210 offset:0x400
	ds_read_b64_tr_b16 v[128:129], v210 offset:0xc00
	v_mfma_f32_32x32x16_bf16 v[50:65], v[82:85], v[130:133], v[50:65]
	ds_read_b64_tr_b16 v[130:131], v210 offset:0x1400
	ds_read_b64_tr_b16 v[132:133], v210 offset:0x1c00
	v_mfma_f32_32x32x16_bf16 v[50:65], v[118:121], v[134:137], v[50:65]
	ds_read_b64_tr_b16 v[134:135], v210 offset:0x2400
	ds_read_b64_tr_b16 v[136:137], v210 offset:0x2c00
	ds_read_b64_tr_b16 v[138:139], v210 offset:0x3400
	ds_read_b64_tr_b16 v[140:141], v210 offset:0x3c00
	s_waitcnt lgkmcnt(0)
	v_mfma_f32_32x32x16_bf16 v[50:65], v[122:125], v[142:145], v[50:65]
	v_mfma_f32_32x32x16_bf16 v[34:49], v[12:15], v[126:129], v[34:49]
	ds_read_b64_tr_b16 v[126:127], v210 offset:0x600
	ds_read_b64_tr_b16 v[128:129], v210 offset:0xe00
	v_mfma_f32_32x32x16_bf16 v[34:49], v[82:85], v[130:133], v[34:49]
	ds_read_b64_tr_b16 v[130:131], v210 offset:0x1600
	ds_read_b64_tr_b16 v[132:133], v210 offset:0x1e00
	v_mfma_f32_32x32x16_bf16 v[34:49], v[118:121], v[134:137], v[34:49]
	ds_read_b64_tr_b16 v[134:135], v210 offset:0x2600
	ds_read_b64_tr_b16 v[136:137], v210 offset:0x2e00
	ds_read_b64_tr_b16 v[142:143], v210 offset:0x3600
	ds_read_b64_tr_b16 v[144:145], v210 offset:0x3e00
	s_waitcnt lgkmcnt(0)
	v_mfma_f32_32x32x16_bf16 v[34:49], v[122:125], v[138:141], v[34:49]
	v_mfma_f32_32x32x16_bf16 v[18:33], v[12:15], v[126:129], v[18:33]
	s_cmp_le_i32 s7, s46
	s_cselect_b64 s[50:51], -1, 0
	s_cmp_gt_i32 s6, s18
	s_cselect_b64 s[6:7], -1, 0
	s_and_b64 s[6:7], s[6:7], s[50:51]
	s_and_b64 vcc, exec, s[6:7]
	v_mfma_f32_32x32x16_bf16 v[18:33], v[82:85], v[130:133], v[18:33]
	v_mfma_f32_32x32x16_bf16 v[18:33], v[118:121], v[134:137], v[18:33]
	v_mfma_f32_32x32x16_bf16 v[18:33], v[122:125], v[142:145], v[18:33]
	s_cbranch_vccnz .LBB0_527
	v_add_u32_e32 v12, 0x7b, v193
	v_cmp_gt_u32_e32 vcc, 2.0, v12
	v_add_u32_e32 v12, 0x5b, v193
	s_nop 0
	v_cndmask_b32_e32 v102, v200, v102, vcc
	v_cmp_gt_u32_e32 vcc, 2.0, v12
	v_add_u32_e32 v12, 0x7a, v193
	s_nop 0
	v_cndmask_b32_e32 v86, v200, v86, vcc
	v_cmp_gt_u32_e32 vcc, 2.0, v12
	v_add_u32_e32 v12, 0x5a, v193
	s_nop 0
	v_cndmask_b32_e32 v103, v200, v103, vcc
	v_cmp_gt_u32_e32 vcc, 2.0, v12
	v_add_u32_e32 v12, 0x79, v193
	s_nop 0
	v_cndmask_b32_e32 v87, v200, v87, vcc
	v_cmp_gt_u32_e32 vcc, 2.0, v12
	v_add_u32_e32 v12, 0x59, v193
	s_nop 0
	v_cndmask_b32_e32 v104, v200, v104, vcc
	v_cmp_gt_u32_e32 vcc, 2.0, v12
	v_add_u32_e32 v12, 0x78, v193
	s_nop 0
	v_cndmask_b32_e32 v88, v200, v88, vcc
	v_cmp_gt_u32_e32 vcc, 2.0, v12
	v_add_u32_e32 v12, 0x58, v193
	s_nop 0
	v_cndmask_b32_e32 v105, v200, v105, vcc
	v_cmp_gt_u32_e32 vcc, 2.0, v12
	v_add_u32_e32 v12, 0x73, v193
	s_nop 0
	v_cndmask_b32_e32 v89, v200, v89, vcc
	v_cmp_gt_u32_e32 vcc, 2.0, v12
	v_add_u32_e32 v12, 0x53, v193
	s_nop 0
	v_cndmask_b32_e32 v106, v200, v106, vcc
	v_cmp_gt_u32_e32 vcc, 2.0, v12
	v_add_u32_e32 v12, 0x72, v193
	s_nop 0
	v_cndmask_b32_e32 v90, v200, v90, vcc
	v_cmp_gt_u32_e32 vcc, 2.0, v12
	v_add_u32_e32 v12, 0x52, v193
	s_nop 0
	v_cndmask_b32_e32 v107, v200, v107, vcc
	v_cmp_gt_u32_e32 vcc, 2.0, v12
	v_add_u32_e32 v12, 0x71, v193
	s_nop 0
	v_cndmask_b32_e32 v91, v200, v91, vcc
	v_cmp_gt_u32_e32 vcc, 2.0, v12
	v_add_u32_e32 v12, 0x51, v193
	s_nop 0
	v_cndmask_b32_e32 v108, v200, v108, vcc
	v_cmp_gt_u32_e32 vcc, 2.0, v12
	v_add_u32_e32 v12, 0x70, v193
	s_nop 0
	v_cndmask_b32_e32 v92, v200, v92, vcc
	v_cmp_gt_u32_e32 vcc, 2.0, v12
	v_add_u32_e32 v12, 0x50, v193
	s_nop 0
	v_cndmask_b32_e32 v109, v200, v109, vcc
	v_cmp_gt_u32_e32 vcc, 2.0, v12
	v_add_u32_e32 v12, 0x6b, v193
	s_nop 0
	v_cndmask_b32_e32 v93, v200, v93, vcc
	v_cmp_gt_u32_e32 vcc, 2.0, v12
	v_add_u32_e32 v12, 0x4b, v193
	s_nop 0
	v_cndmask_b32_e32 v110, v200, v110, vcc
	v_cmp_gt_u32_e32 vcc, 2.0, v12
	v_add_u32_e32 v12, 0x6a, v193
	s_nop 0
	v_cndmask_b32_e32 v94, v200, v94, vcc
	v_cmp_gt_u32_e32 vcc, 2.0, v12
	v_add_u32_e32 v12, 0x4a, v193
	s_nop 0
	v_cndmask_b32_e32 v111, v200, v111, vcc
	v_cmp_gt_u32_e32 vcc, 2.0, v12
	v_add_u32_e32 v12, 0x69, v193
	s_nop 0
	v_cndmask_b32_e32 v95, v200, v95, vcc
	v_cmp_gt_u32_e32 vcc, 2.0, v12
	v_add_u32_e32 v12, 0x49, v193
	s_nop 0
	v_cndmask_b32_e32 v112, v200, v112, vcc
	v_cmp_gt_u32_e32 vcc, 2.0, v12
	v_add_u32_e32 v12, 0x68, v193
	s_nop 0
	v_cndmask_b32_e32 v96, v200, v96, vcc
	v_cmp_gt_u32_e32 vcc, 2.0, v12
	v_add_u32_e32 v12, 0x48, v193
	s_nop 0
	v_cndmask_b32_e32 v113, v200, v113, vcc
	v_cmp_gt_u32_e32 vcc, 2.0, v12
	v_add_u32_e32 v12, 0x63, v193
	s_nop 0
	v_cndmask_b32_e32 v97, v200, v97, vcc
	v_cmp_gt_u32_e32 vcc, 2.0, v12
	v_add_u32_e32 v12, 0x43, v193
	s_nop 0
	v_cndmask_b32_e32 v114, v200, v114, vcc
	v_cmp_gt_u32_e32 vcc, 2.0, v12
	v_add_u32_e32 v12, 0x62, v193
	s_nop 0
	v_cndmask_b32_e32 v98, v200, v98, vcc
	v_cmp_gt_u32_e32 vcc, 2.0, v12
	v_add_u32_e32 v12, 0x42, v193
	s_nop 0
	v_cndmask_b32_e32 v115, v200, v115, vcc
	v_cmp_gt_u32_e32 vcc, 2.0, v12
	v_add_u32_e32 v12, 0x61, v193
	s_nop 0
	v_cndmask_b32_e32 v99, v200, v99, vcc
	v_cmp_gt_u32_e32 vcc, 2.0, v12
	v_add_u32_e32 v12, 0x41, v193
	s_nop 0
	v_cndmask_b32_e32 v116, v200, v116, vcc
	v_cmp_gt_u32_e32 vcc, 2.0, v12
	v_add_u32_e32 v12, 0x60, v193
	s_nop 0
	v_cndmask_b32_e32 v100, v200, v100, vcc
	v_cmp_gt_u32_e32 vcc, 2.0, v12
	v_add_u32_e32 v12, 64, v193
	s_nop 0
	v_cndmask_b32_e32 v117, v200, v117, vcc
	v_cmp_gt_u32_e32 vcc, 2.0, v12
	s_nop 1
	v_cndmask_b32_e32 v101, v200, v101, vcc

; __device__ __forceinline__ void finishSM(f32x16& p0, f32x16& p1, float alpha, float& l_reg, bf16x8& pa0, bf16x8& pa1, bf16x8& pa2, bf16x8& pa3) {
; #pragma unroll
;     for (int r = 0; r < 16; ++r) p1[r] = __builtin_amdgcn_exp2f(p1[r]);
;     float ps = 0;
; #pragma unroll
;     for (int r = 0; r < 16; ++r) ps += p0[r];
; #pragma unroll
;     for (int r = 0; r < 16; ++r) ps += p1[r];
;     { auto rr = __builtin_amdgcn_permlane32_swap(__float_as_uint(ps), __float_as_uint(ps), false, false);
;       ps = __uint_as_float(rr[0]) + __uint_as_float(rr[1]); }
;     l_reg = l_reg * alpha + ps;
;     ...
;     PK4(p0, 0, pa0); PK4(p0, 8, pa1); PK4(p1, 0, pa2); PK4(p1, 8, pa3);
; template <int KB, bool SK, bool ROPE, bool QHALF>
; __device__ __forceinline__ void qkt(f32x16& p0, f32x16& p1, const char* lds, int r32, int hi, const bf16x8* qr, const char* qrl, bool act) {
;     ...
;     const char* kb[4];
; #pragma unroll
;     for (int dd = 0; dd < 4; ++dd) kb[dd] = lds + OFF_K + KB * SHM_K + KSWZ(r32, (dd * 16 + hi * 8) * 2);
; #pragma unroll
;     for (int d0 = 0; d0 < 8; ++d0) { const char* a = kb[d0 & 3] + (d0 >> 2) * 128;
;         bf16x8 b0 = *reinterpret_cast<const bf16x8*>(a);
;         bf16x8 b1 = *reinterpret_cast<const bf16x8*>(a + 32 * 256);
;         bf16x8 qf;
;         if constexpr (QHALF) { if (d0 >= 4) qf = *reinterpret_cast<const bf16x8*>(qrl + (d0 - 4) * 1024); else qf = qr[d0]; } else qf = qr[d0];
;         p0 = __builtin_amdgcn_mfma_f32_32x32x16_bf16(b0, qf, p0, 0, 0, 0);
;         p1 = __builtin_amdgcn_mfma_f32_32x32x16_bf16(b1, qf, p1, 0, 0, 0); }
;     if constexpr (ROPE) {
; #pragma unroll
;         for (int d0 = 0; d0 < 4; ++d0) { const char* a = lds + OFF_KR + KB * SHM_KR + KRSWZ(r32, 2 * d0 + hi);
;             bf16x8 b0 = *reinterpret_cast<const bf16x8*>(a);
;             bf16x8 b1 = *reinterpret_cast<const bf16x8*>(a + 32 * 128);
;             const bf16x8 qf = *reinterpret_cast<const bf16x8*>(qrl + d0 * 1024);
;             p0 = __builtin_amdgcn_mfma_f32_32x32x16_bf16(b0, qf, p0, 0, 0, 0);
;             p1 = __builtin_amdgcn_mfma_f32_32x32x16_bf16(b1, qf, p1, 0, 0, 0); }
.Lmy_nobar_1:
.LBB0_1036:
	ds_read_b128 v[4:7], v212 offset:49152
	ds_read_b128 v[8:11], v212 offset:57344
	s_add_i32 s10, 0, 0x12800
	v_exp_f32_e32 v122, v132
	v_exp_f32_e32 v123, v133
	s_waitcnt lgkmcnt(1)
	v_mfma_f32_32x32x16_bf16 v[102:117], v[4:7], v[174:177], 0
	v_exp_f32_e32 v124, v130
	v_exp_f32_e32 v125, v131
	v_exp_f32_e32 v126, v126
	v_exp_f32_e32 v127, v127
	v_exp_f32_e32 v128, v128
	v_exp_f32_e32 v129, v129
	s_add_i32 s6, s42, 0xffffff60
	s_waitcnt lgkmcnt(0)
	v_mfma_f32_32x32x16_bf16 v[86:101], v[8:11], v[174:177], 0
	ds_read_b128 v[4:7], v213 offset:49152
	ds_read_b128 v[8:11], v213 offset:57344
	s_add_i32 s7, s42, 0xffffff9f
	s_waitcnt lgkmcnt(1)
	v_mfma_f32_32x32x16_bf16 v[102:117], v[4:7], v[170:173], v[102:117]
	s_waitcnt lgkmcnt(0)
	v_mfma_f32_32x32x16_bf16 v[86:101], v[8:11], v[170:173], v[86:101]
	ds_read_b128 v[4:7], v214 offset:49152
	ds_read_b128 v[8:11], v214 offset:57344
	s_waitcnt lgkmcnt(1)
	v_mfma_f32_32x32x16_bf16 v[102:117], v[4:7], v[166:169], v[102:117]
	s_waitcnt lgkmcnt(0)
	v_mfma_f32_32x32x16_bf16 v[86:101], v[8:11], v[166:169], v[86:101]
	ds_read_b128 v[4:7], v215 offset:49152
	ds_read_b128 v[8:11], v215 offset:57344
	s_waitcnt lgkmcnt(1)
	v_mfma_f32_32x32x16_bf16 v[102:117], v[4:7], v[162:165], v[102:117]
	s_waitcnt lgkmcnt(0)
	v_mfma_f32_32x32x16_bf16 v[86:101], v[8:11], v[162:165], v[86:101]
	ds_read_b128 v[4:7], v212 offset:49280
	ds_read_b128 v[8:11], v212 offset:57472
	s_waitcnt lgkmcnt(1)
	v_mfma_f32_32x32x16_bf16 v[102:117], v[4:7], v[158:161], v[102:117]
	s_waitcnt lgkmcnt(0)
	v_mfma_f32_32x32x16_bf16 v[86:101], v[8:11], v[158:161], v[86:101]
	ds_read_b128 v[4:7], v213 offset:49280
	ds_read_b128 v[8:11], v213 offset:57472
	s_waitcnt lgkmcnt(1)
	v_mfma_f32_32x32x16_bf16 v[102:117], v[4:7], v[154:157], v[102:117]
	s_waitcnt lgkmcnt(0)
	v_mfma_f32_32x32x16_bf16 v[86:101], v[8:11], v[154:157], v[86:101]
	ds_read_b128 v[4:7], v214 offset:49280
	ds_read_b128 v[8:11], v214 offset:57472
	s_waitcnt lgkmcnt(1)
	v_mfma_f32_32x32x16_bf16 v[102:117], v[4:7], v[150:153], v[102:117]
	s_waitcnt lgkmcnt(0)
	v_mfma_f32_32x32x16_bf16 v[86:101], v[8:11], v[150:153], v[86:101]
	ds_read_b128 v[4:7], v215 offset:49280
	ds_read_b128 v[8:11], v215 offset:57472
	s_waitcnt lgkmcnt(1)
	v_mfma_f32_32x32x16_bf16 v[102:117], v[4:7], v[146:149], v[102:117]
	s_waitcnt lgkmcnt(0)
	v_mfma_f32_32x32x16_bf16 v[86:101], v[8:11], v[146:149], v[86:101]
	v_add_u32_e32 v8, s10, v216
	ds_read_b128 v[4:7], v8
	ds_read_b128 v[8:11], v8 offset:4096
	ds_read_b128 v[12:15], v202
	s_waitcnt lgkmcnt(0)
	v_mfma_f32_32x32x16_bf16 v[102:117], v[4:7], v[12:15], v[102:117]
	v_mfma_f32_32x32x16_bf16 v[86:101], v[8:11], v[12:15], v[86:101]
	v_add_u32_e32 v8, s10, v217
	ds_read_b128 v[4:7], v8
	ds_read_b128 v[8:11], v8 offset:4096
	ds_read_b128 v[12:15], v202 offset:1024
	s_waitcnt lgkmcnt(0)
	v_mfma_f32_32x32x16_bf16 v[102:117], v[4:7], v[12:15], v[102:117]
	v_mfma_f32_32x32x16_bf16 v[86:101], v[8:11], v[12:15], v[86:101]
	v_add_u32_e32 v8, s10, v218
	ds_read_b128 v[4:7], v8
	ds_read_b128 v[8:11], v8 offset:4096
	ds_read_b128 v[12:15], v202 offset:2048
	s_waitcnt lgkmcnt(0)
	v_mfma_f32_32x32x16_bf16 v[102:117], v[4:7], v[12:15], v[102:117]
	v_mfma_f32_32x32x16_bf16 v[86:101], v[8:11], v[12:15], v[86:101]
	v_add_u32_e32 v8, s10, v219
	ds_read_b128 v[4:7], v8
	ds_read_b128 v[8:11], v8 offset:4096
	ds_read_b128 v[12:15], v202 offset:3072
	s_waitcnt lgkmcnt(0)
	v_mfma_f32_32x32x16_bf16 v[102:117], v[4:7], v[12:15], v[102:117]
	v_exp_f32_e32 v4, v140
	v_exp_f32_e32 v5, v141
	v_exp_f32_e32 v6, v138
	v_exp_f32_e32 v7, v139
	v_mfma_f32_32x32x16_bf16 v[86:101], v[8:11], v[12:15], v[86:101]
	ds_read_b64_tr_b16 v[230:231], v209 offset:0
	ds_read_b64_tr_b16 v[232:233], v209 offset:0x800
	ds_read_b64_tr_b16 v[234:235], v209 offset:0x1000
	ds_read_b64_tr_b16 v[236:237], v209 offset:0x1800
	ds_read_b64_tr_b16 v[238:239], v209 offset:0x2000
	ds_read_b64_tr_b16 v[240:241], v209 offset:0x2800
	ds_read_b64_tr_b16 v[242:243], v209 offset:0x3000
	ds_read_b64_tr_b16 v[244:245], v209 offset:0x3800
	v_add_f32_e32 v12, 0, v188
	v_add_f32_e32 v12, v227, v12
	v_add_f32_e32 v12, v186, v12
	v_add_f32_e32 v12, v189, v12
	v_add_f32_e32 v12, v185, v12
	v_add_f32_e32 v12, v187, v12
	v_add_f32_e32 v12, v183, v12
	v_add_f32_e32 v12, v184, v12
	v_add_f32_e32 v12, v179, v12
	v_add_f32_e32 v12, v182, v12
	v_add_f32_e32 v12, v144, v12
	v_add_f32_e32 v12, v180, v12
	v_add_f32_e32 v12, v142, v12
	v_add_f32_e32 v12, v181, v12
	v_add_f32_e32 v12, v143, v12
	v_add_f32_e32 v12, v145, v12
	v_exp_f32_e32 v8, v136
	v_exp_f32_e32 v9, v137
	v_exp_f32_e32 v10, v134
	v_exp_f32_e32 v11, v135
	v_pk_add_f32 v[14:15], v[4:5], v[6:7]
	v_pk_add_f32 v[14:15], v[14:15], v[8:9]
	v_pk_add_f32 v[14:15], v[14:15], v[10:11]
	v_pk_add_f32 v[14:15], v[14:15], v[122:123]
	v_pk_add_f32 v[14:15], v[14:15], v[124:125]
	v_pk_add_f32 v[14:15], v[14:15], v[126:127]
	v_pk_add_f32 v[14:15], v[14:15], v[128:129]
	v_add_f32_e32 v12, v14, v12
	v_add_f32_e32 v195, v15, v12
	v_mov_b32_e32 v225, v195
	s_nop 1
	v_permlane32_swap_b32_e32 v195, v225
	v_cvt_pk_bf16_f32 v12, v188, v227
	v_cvt_pk_bf16_f32 v13, v186, v189
	v_cvt_pk_bf16_f32 v14, v185, v187
	v_cvt_pk_bf16_f32 v15, v183, v184
	v_cvt_pk_bf16_f32 v82, v179, v182
	v_cvt_pk_bf16_f32 v83, v144, v180
	v_cvt_pk_bf16_f32 v84, v142, v181
	v_cvt_pk_bf16_f32 v85, v143, v145
	v_cvt_pk_bf16_f32 v118, v4, v5
	v_cvt_pk_bf16_f32 v119, v6, v7
	v_cvt_pk_bf16_f32 v120, v8, v9
	v_cvt_pk_bf16_f32 v121, v10, v11
	v_cvt_pk_bf16_f32 v122, v122, v123
	v_cvt_pk_bf16_f32 v123, v124, v125
	v_cvt_pk_bf16_f32 v124, v126, v127
	v_cvt_pk_bf16_f32 v125, v128, v129
	s_nop 0
	v_permlane32_swap_b32_e32 v12, v14
	v_permlane32_swap_b32_e32 v13, v15
	v_permlane32_swap_b32_e32 v82, v84
	v_permlane32_swap_b32_e32 v83, v85
	v_permlane32_swap_b32_e32 v118, v120
	v_permlane32_swap_b32_e32 v119, v121
	v_permlane32_swap_b32_e32 v122, v124
	v_permlane32_swap_b32_e32 v123, v125
	s_add_i32 s10, s42, 0xffffffa0
	s_sub_i32 s64, s42, 64
	s_mov_b32 s65, s11
	s_lshl_b64 s[44:45], s[10:11], 12
	s_lshl_b64 s[64:65], s[64:65], 12
	v_lshl_add_u64 v[4:5], v[196:197], 0, s[44:45]
	v_lshl_add_u64 v[8:9], v[196:197], 0, s[64:65]
	v_lshl_add_u64 v[126:127], v[198:199], 0, s[44:45]
	s_add_i32 m0, s37, 0x8000
	global_load_dwordx4 v[4:7], v[4:5], off
	s_nop 0
	global_load_dwordx4 v[8:11], v[8:9], off
	s_lshl_b64 s[44:45], s[10:11], 7
	global_load_lds_dwordx4 v[126:127], off
	v_lshl_add_u64 v[126:127], v[198:199], 0, s[64:65]
	s_add_i32 m0, s37, 0xa000
	s_nop 0
	global_load_lds_dwordx4 v[126:127], off
	v_lshl_add_u64 v[126:127], v[16:17], 0, s[44:45]
	s_add_i32 m0, s37, 0x10800
	s_nop 0
	global_load_lds_dwordx4 v[126:127], off
	s_waitcnt lgkmcnt(0)
; __device__ __forceinline__ void mask_tile(f32x16& p0, f32x16& p1, int dq, unsigned W) {
;     const float NEG = -__builtin_inff();
; #pragma unroll
;     for (int r = 0; r < 16; ++r) {
;         const int c = (r & 3) + 8 * (r >> 2);
;         if ((unsigned)(dq - c) >= W) p0[r] = NEG;
;         if ((unsigned)(dq - c - 32) >= W) p1[r] = NEG;
;     }
; }
; template <int VB, bool SK>
; __device__ __forceinline__ void pv_tile(f32x16* o, int vb0, bf16x8 pa0, bf16x8 pa1, bf16x8 pa2, bf16x8 pa3, bool act) {
;     if (SK && !act) return;
;     ...
;     if (ATT_PRIO) __builtin_amdgcn_s_setprio(1);
;     PV_D0(0); PV_D0(1); PV_D0(2); PV_D0(3);
	s_nop 0
	v_mfma_f32_32x32x16_bf16 v[66:81], v[12:15], v[230:233], v[66:81]
	ds_read_b64_tr_b16 v[126:127], v209 offset:0x200
	ds_read_b64_tr_b16 v[128:129], v209 offset:0xa00
	v_mfma_f32_32x32x16_bf16 v[66:81], v[82:85], v[234:237], v[66:81]
	ds_read_b64_tr_b16 v[130:131], v209 offset:0x1200
	ds_read_b64_tr_b16 v[132:133], v209 offset:0x1a00
	v_mfma_f32_32x32x16_bf16 v[66:81], v[118:121], v[238:241], v[66:81]
	ds_read_b64_tr_b16 v[134:135], v209 offset:0x2200
	ds_read_b64_tr_b16 v[136:137], v209 offset:0x2a00
	ds_read_b64_tr_b16 v[142:143], v209 offset:0x3200
	ds_read_b64_tr_b16 v[144:145], v209 offset:0x3a00
	s_waitcnt lgkmcnt(0)
	v_mfma_f32_32x32x16_bf16 v[66:81], v[122:125], v[242:245], v[66:81]
	v_mfma_f32_32x32x16_bf16 v[50:65], v[12:15], v[126:129], v[50:65]
	ds_read_b64_tr_b16 v[126:127], v209 offset:0x400
	ds_read_b64_tr_b16 v[128:129], v209 offset:0xc00
	v_mfma_f32_32x32x16_bf16 v[50:65], v[82:85], v[130:133], v[50:65]
	ds_read_b64_tr_b16 v[130:131], v209 offset:0x1400
	ds_read_b64_tr_b16 v[132:133], v209 offset:0x1c00
	v_mfma_f32_32x32x16_bf16 v[50:65], v[118:121], v[134:137], v[50:65]
	ds_read_b64_tr_b16 v[134:135], v209 offset:0x2400
	ds_read_b64_tr_b16 v[136:137], v209 offset:0x2c00
	ds_read_b64_tr_b16 v[138:139], v209 offset:0x3400
	ds_read_b64_tr_b16 v[140:141], v209 offset:0x3c00
	s_waitcnt lgkmcnt(0)
	v_mfma_f32_32x32x16_bf16 v[50:65], v[122:125], v[142:145], v[50:65]
	v_mfma_f32_32x32x16_bf16 v[34:49], v[12:15], v[126:129], v[34:49]
	ds_read_b64_tr_b16 v[126:127], v209 offset:0x600
	ds_read_b64_tr_b16 v[128:129], v209 offset:0xe00
	v_mfma_f32_32x32x16_bf16 v[34:49], v[82:85], v[130:133], v[34:49]
	ds_read_b64_tr_b16 v[130:131], v209 offset:0x1600
	ds_read_b64_tr_b16 v[132:133], v209 offset:0x1e00
	v_mfma_f32_32x32x16_bf16 v[34:49], v[118:121], v[134:137], v[34:49]
	ds_read_b64_tr_b16 v[134:135], v209 offset:0x2600
	ds_read_b64_tr_b16 v[136:137], v209 offset:0x2e00
	ds_read_b64_tr_b16 v[142:143], v209 offset:0x3600
	ds_read_b64_tr_b16 v[144:145], v209 offset:0x3e00
	s_waitcnt lgkmcnt(0)
	v_mfma_f32_32x32x16_bf16 v[34:49], v[122:125], v[138:141], v[34:49]
	v_mfma_f32_32x32x16_bf16 v[18:33], v[12:15], v[126:129], v[18:33]
	s_cmp_le_i32 s7, s40
	s_cselect_b64 s[44:45], -1, 0
	s_cmp_gt_i32 s6, s60
	s_cselect_b64 s[6:7], -1, 0
	s_and_b64 s[6:7], s[6:7], s[44:45]
	s_and_b64 vcc, exec, s[6:7]
	v_mfma_f32_32x32x16_bf16 v[18:33], v[82:85], v[130:133], v[18:33]
	v_mfma_f32_32x32x16_bf16 v[18:33], v[118:121], v[134:137], v[18:33]
	v_mfma_f32_32x32x16_bf16 v[18:33], v[122:125], v[142:145], v[18:33]
	s_cbranch_vccnz .LBB0_1038
	v_add_u32_e32 v12, 0x7b, v193
	v_cmp_gt_u32_e32 vcc, 2.0, v12
	v_add_u32_e32 v12, 0x5b, v193
	s_nop 0
	v_cndmask_b32_e32 v102, v200, v102, vcc
	v_cmp_gt_u32_e32 vcc, 2.0, v12
	v_add_u32_e32 v12, 0x7a, v193
	s_nop 0
	v_cndmask_b32_e32 v86, v200, v86, vcc
	v_cmp_gt_u32_e32 vcc, 2.0, v12
	v_add_u32_e32 v12, 0x5a, v193
	s_nop 0
	v_cndmask_b32_e32 v103, v200, v103, vcc
	v_cmp_gt_u32_e32 vcc, 2.0, v12
	v_add_u32_e32 v12, 0x79, v193
	s_nop 0
	v_cndmask_b32_e32 v87, v200, v87, vcc
	v_cmp_gt_u32_e32 vcc, 2.0, v12
	v_add_u32_e32 v12, 0x59, v193
	s_nop 0
	v_cndmask_b32_e32 v104, v200, v104, vcc
	v_cmp_gt_u32_e32 vcc, 2.0, v12
	v_add_u32_e32 v12, 0x78, v193
	s_nop 0
	v_cndmask_b32_e32 v88, v200, v88, vcc
	v_cmp_gt_u32_e32 vcc, 2.0, v12
	v_add_u32_e32 v12, 0x58, v193
	s_nop 0
	v_cndmask_b32_e32 v105, v200, v105, vcc
	v_cmp_gt_u32_e32 vcc, 2.0, v12
	v_add_u32_e32 v12, 0x73, v193
	s_nop 0
	v_cndmask_b32_e32 v89, v200, v89, vcc
	v_cmp_gt_u32_e32 vcc, 2.0, v12
	v_add_u32_e32 v12, 0x53, v193
	s_nop 0
	v_cndmask_b32_e32 v106, v200, v106, vcc
	v_cmp_gt_u32_e32 vcc, 2.0, v12
	v_add_u32_e32 v12, 0x72, v193
	s_nop 0
	v_cndmask_b32_e32 v90, v200, v90, vcc
	v_cmp_gt_u32_e32 vcc, 2.0, v12
	v_add_u32_e32 v12, 0x52, v193
	s_nop 0
	v_cndmask_b32_e32 v107, v200, v107, vcc
	v_cmp_gt_u32_e32 vcc, 2.0, v12
	v_add_u32_e32 v12, 0x71, v193
	s_nop 0
	v_cndmask_b32_e32 v91, v200, v91, vcc
	v_cmp_gt_u32_e32 vcc, 2.0, v12
	v_add_u32_e32 v12, 0x51, v193
	s_nop 0
	v_cndmask_b32_e32 v108, v200, v108, vcc
	v_cmp_gt_u32_e32 vcc, 2.0, v12
	v_add_u32_e32 v12, 0x70, v193
	s_nop 0
	v_cndmask_b32_e32 v92, v200, v92, vcc
	v_cmp_gt_u32_e32 vcc, 2.0, v12
	v_add_u32_e32 v12, 0x50, v193
	s_nop 0
	v_cndmask_b32_e32 v109, v200, v109, vcc
	v_cmp_gt_u32_e32 vcc, 2.0, v12
	v_add_u32_e32 v12, 0x6b, v193
	s_nop 0
	v_cndmask_b32_e32 v93, v200, v93, vcc
	v_cmp_gt_u32_e32 vcc, 2.0, v12
	v_add_u32_e32 v12, 0x4b, v193
	s_nop 0
	v_cndmask_b32_e32 v110, v200, v110, vcc
	v_cmp_gt_u32_e32 vcc, 2.0, v12
	v_add_u32_e32 v12, 0x6a, v193
	s_nop 0
	v_cndmask_b32_e32 v94, v200, v94, vcc
	v_cmp_gt_u32_e32 vcc, 2.0, v12
	v_add_u32_e32 v12, 0x4a, v193
	s_nop 0
	v_cndmask_b32_e32 v111, v200, v111, vcc
	v_cmp_gt_u32_e32 vcc, 2.0, v12
	v_add_u32_e32 v12, 0x69, v193
	s_nop 0
	v_cndmask_b32_e32 v95, v200, v95, vcc
	v_cmp_gt_u32_e32 vcc, 2.0, v12
	v_add_u32_e32 v12, 0x49, v193
	s_nop 0
	v_cndmask_b32_e32 v112, v200, v112, vcc
	v_cmp_gt_u32_e32 vcc, 2.0, v12
	v_add_u32_e32 v12, 0x68, v193
	s_nop 0
	v_cndmask_b32_e32 v96, v200, v96, vcc
	v_cmp_gt_u32_e32 vcc, 2.0, v12
	v_add_u32_e32 v12, 0x48, v193
	s_nop 0
	v_cndmask_b32_e32 v113, v200, v113, vcc
	v_cmp_gt_u32_e32 vcc, 2.0, v12
	v_add_u32_e32 v12, 0x63, v193
	s_nop 0
	v_cndmask_b32_e32 v97, v200, v97, vcc
	v_cmp_gt_u32_e32 vcc, 2.0, v12
	v_add_u32_e32 v12, 0x43, v193
	s_nop 0
	v_cndmask_b32_e32 v114, v200, v114, vcc
	v_cmp_gt_u32_e32 vcc, 2.0, v12
	v_add_u32_e32 v12, 0x62, v193
	s_nop 0
	v_cndmask_b32_e32 v98, v200, v98, vcc
	v_cmp_gt_u32_e32 vcc, 2.0, v12
	v_add_u32_e32 v12, 0x42, v193
	s_nop 0
	v_cndmask_b32_e32 v115, v200, v115, vcc
	v_cmp_gt_u32_e32 vcc, 2.0, v12
	v_add_u32_e32 v12, 0x61, v193
	s_nop 0
	v_cndmask_b32_e32 v99, v200, v99, vcc
	v_cmp_gt_u32_e32 vcc, 2.0, v12
	v_add_u32_e32 v12, 0x41, v193
	s_nop 0
	v_cndmask_b32_e32 v116, v200, v116, vcc
	v_cmp_gt_u32_e32 vcc, 2.0, v12
	v_add_u32_e32 v12, 0x60, v193
	s_nop 0
	v_cndmask_b32_e32 v100, v200, v100, vcc
	v_cmp_gt_u32_e32 vcc, 2.0, v12
	v_add_u32_e32 v12, 64, v193
	s_nop 0
	v_cndmask_b32_e32 v117, v200, v117, vcc
	v_cmp_gt_u32_e32 vcc, 2.0, v12
	s_nop 1
	v_cndmask_b32_e32 v101, v200, v101, vcc
